# speedup vs baseline: 1.0030x; 1.0030x over previous
.LBB3_16:
	v_max_f32_e32 v36, 0xf149f2ca, v2
	v_cndmask_b32_e64 v194, v36, v217, s[0:1]
	v_mul_f32_e32 v2, 0xbe0293ee, v194
	v_fmamk_f32 v20, v20, 0x3e0293ee, v2
	v_exp_f32_e32 v143, v20
	v_sub_f32_e32 v20, 0xf149f2ca, v36
	v_mul_f32_e32 v20, 0x3e0293ee, v20
	v_fmamk_f32 v21, v21, 0x3e0293ee, v2
	v_fmamk_f32 v22, v22, 0x3e0293ee, v2
	v_fmamk_f32 v23, v23, 0x3e0293ee, v2
	v_fmamk_f32 v24, v24, 0x3e0293ee, v2
	v_fmamk_f32 v25, v25, 0x3e0293ee, v2
	v_fmamk_f32 v26, v26, 0x3e0293ee, v2
	v_fmamk_f32 v27, v27, 0x3e0293ee, v2
	v_fmamk_f32 v28, v28, 0x3e0293ee, v2
	v_fmamk_f32 v29, v29, 0x3e0293ee, v2
	v_fmamk_f32 v30, v30, 0x3e0293ee, v2
	v_fmamk_f32 v31, v31, 0x3e0293ee, v2
	v_fmamk_f32 v32, v32, 0x3e0293ee, v2
	v_fmamk_f32 v33, v33, 0x3e0293ee, v2
	v_fmamk_f32 v34, v34, 0x3e0293ee, v2
	v_fmamk_f32 v35, v35, 0x3e0293ee, v2
	v_exp_f32_e32 v20, v20
	v_exp_f32_e32 v145, v21
	v_exp_f32_e32 v141, v22
	v_exp_f32_e32 v144, v23
	v_exp_f32_e32 v140, v24
	v_exp_f32_e32 v142, v25
	v_exp_f32_e32 v138, v26
	v_exp_f32_e32 v139, v27
	v_exp_f32_e32 v133, v28
	v_exp_f32_e32 v136, v29
	v_exp_f32_e32 v131, v30
	v_exp_f32_e32 v134, v31
	v_exp_f32_e32 v130, v32
	v_exp_f32_e32 v137, v33
	v_exp_f32_e32 v132, v34
	v_exp_f32_e32 v135, v35
	v_cndmask_b32_e64 v219, v20, 1.0, s[0:1]
	v_pk_fma_f32 v[128:129], v[18:19], s[18:19], v[2:3] op_sel_hi:[1,0,0]
	v_pk_fma_f32 v[126:127], v[16:17], s[18:19], v[2:3] op_sel_hi:[1,0,0]
	v_pk_fma_f32 v[124:125], v[14:15], s[18:19], v[2:3] op_sel_hi:[1,0,0]
	v_pk_fma_f32 v[122:123], v[12:13], s[18:19], v[2:3] op_sel_hi:[1,0,0]
	v_pk_fma_f32 v[120:121], v[10:11], s[18:19], v[2:3] op_sel_hi:[1,0,0]
	v_pk_fma_f32 v[118:119], v[8:9], s[18:19], v[2:3] op_sel_hi:[1,0,0]
	v_pk_fma_f32 v[116:117], v[6:7], s[18:19], v[2:3] op_sel_hi:[1,0,0]
	v_pk_fma_f32 v[114:115], v[4:5], s[18:19], v[2:3] op_sel_hi:[1,0,0]
	s_cmp_lt_i32 s48, 3
	s_waitcnt lgkmcnt(0)
	s_barrier
	s_cbranch_scc1 .LBB3_31
	s_add_i32 s0, s47, s51
	v_mov_b32_e32 v220, 0
	v_mov_b32_e32 v246, v182
	v_mov_b32_e32 v247, v183
	v_mov_b32_e32 v248, v184
	v_mov_b32_e32 v249, v185
	v_mov_b32_e32 v250, v178
	v_mov_b32_e32 v251, v179
	v_mov_b32_e32 v252, v180
	v_mov_b32_e32 v253, v181
	v_add_u32_e32 v221, s0, v215
	s_movk_i32 s14, 0xbf
	s_mov_b32 s51, 2
	v_mov_b32_e32 v18, 0
	v_mov_b32_e32 v19, v220
	v_mov_b32_e32 v20, v220
	v_mov_b32_e32 v21, v220
	v_mov_b32_e32 v22, v220
	v_mov_b32_e32 v23, v220
	v_mov_b32_e32 v24, v220
	v_mov_b32_e32 v25, v220
	v_mov_b32_e32 v26, v220
	v_mov_b32_e32 v27, v220
	v_mov_b32_e32 v28, v220
	v_mov_b32_e32 v29, v220
	v_mov_b32_e32 v30, v220
	v_mov_b32_e32 v31, v220
	v_mov_b32_e32 v32, v220
	v_mov_b32_e32 v33, v220
	v_mov_b32_e32 v34, 0
	v_mov_b32_e32 v35, v220
	v_mov_b32_e32 v36, v220
	v_mov_b32_e32 v37, v220
	v_mov_b32_e32 v38, v220
	v_mov_b32_e32 v39, v220
	v_mov_b32_e32 v40, v220
	v_mov_b32_e32 v41, v220
	v_mov_b32_e32 v42, v220
	v_mov_b32_e32 v43, v220
	v_mov_b32_e32 v44, v220
	v_mov_b32_e32 v45, v220
	v_mov_b32_e32 v46, v220
	v_mov_b32_e32 v47, v220
	v_mov_b32_e32 v48, v220
	v_mov_b32_e32 v49, v220
	v_mov_b32_e32 v50, 0
	v_mov_b32_e32 v51, v220
	v_mov_b32_e32 v52, v220
	v_mov_b32_e32 v53, v220
	v_mov_b32_e32 v54, v220
	v_mov_b32_e32 v55, v220
	v_mov_b32_e32 v56, v220
	v_mov_b32_e32 v57, v220
	v_mov_b32_e32 v58, v220
	v_mov_b32_e32 v59, v220
	v_mov_b32_e32 v60, v220
	v_mov_b32_e32 v61, v220
	v_mov_b32_e32 v62, v220
	v_mov_b32_e32 v63, v220
	v_mov_b32_e32 v64, v220
	v_mov_b32_e32 v65, v220
	v_mov_b32_e32 v66, 0
	v_mov_b32_e32 v67, v220
	v_mov_b32_e32 v68, v220
	v_mov_b32_e32 v69, v220
	v_mov_b32_e32 v70, v220
	v_mov_b32_e32 v71, v220
	v_mov_b32_e32 v72, v220
	v_mov_b32_e32 v73, v220
	v_mov_b32_e32 v74, v220
	v_mov_b32_e32 v75, v220
	v_mov_b32_e32 v76, v220
	v_mov_b32_e32 v77, v220
	v_mov_b32_e32 v78, v220
	v_mov_b32_e32 v79, v220
	v_mov_b32_e32 v80, v220
	v_mov_b32_e32 v81, v220
	s_branch .LBB3_19

.LBB3_19:
	ds_write_b128 v212, v[246:249] offset:16384
	ds_write_b128 v213, v[250:253] offset:16384
	ds_read_b128 v[4:7], v208 offset:49152
	ds_read_b128 v[8:11], v208 offset:49280
	v_exp_f32_e32 v2, v114
	v_exp_f32_e32 v16, v115
	v_exp_f32_e32 v17, v116
	s_waitcnt lgkmcnt(1)
	v_mfma_f32_32x32x16_f16 v[98:113], v[4:7], v[146:149], 0
	ds_read_b128 v[4:7], v208 offset:57344
	ds_read_b128 v[12:15], v208 offset:57472
	v_exp_f32_e32 v114, v117
	v_exp_f32_e32 v115, v118
	v_exp_f32_e32 v116, v119
	v_exp_f32_e32 v117, v120
	v_exp_f32_e32 v118, v121
	v_exp_f32_e32 v119, v122
	s_waitcnt lgkmcnt(1)
	v_mfma_f32_32x32x16_f16 v[82:97], v[4:7], v[146:149], 0
	ds_read_b128 v[4:7], v209 offset:49152
	s_waitcnt vmcnt(2)
	ds_read_b128 v[178:181], v209 offset:57344
	ds_read_b128 v[182:185], v209 offset:49280
	v_exp_f32_e32 v120, v123
	v_exp_f32_e32 v121, v124
	v_exp_f32_e32 v122, v125
	v_exp_f32_e32 v123, v126
	v_exp_f32_e32 v124, v127
	v_exp_f32_e32 v125, v128
	s_waitcnt lgkmcnt(2)
	v_mfma_f32_32x32x16_f16 v[98:113], v[4:7], v[150:153], v[98:113]
	s_waitcnt vmcnt(1)
	ds_read_b128 v[186:189], v209 offset:57472
	ds_read_b128 v[4:7], v210 offset:49152
	s_waitcnt vmcnt(0)
	ds_read_b128 v[190:193], v210 offset:49280
	ds_read_b128 v[222:225], v210 offset:57344
	ds_read_b128 v[226:229], v210 offset:57472
	ds_read_b128 v[230:233], v211 offset:49152
	ds_read_b128 v[234:237], v211 offset:49280
	v_exp_f32_e32 v126, v129
	s_waitcnt lgkmcnt(8)
	v_mfma_f32_32x32x16_f16 v[82:97], v[178:181], v[150:153], v[82:97]
	ds_read_b128 v[178:181], v211 offset:57344
	ds_read_b128 v[238:241], v211 offset:57472
	s_waitcnt lgkmcnt(7)
	v_mfma_f32_32x32x16_f16 v[98:113], v[4:7], v[154:157], v[98:113]
	v_add_f32_e32 v4, 0, v143
	v_add_f32_e32 v4, v145, v4
	v_add_f32_e32 v4, v141, v4
	v_add_f32_e32 v4, v144, v4
	v_add_f32_e32 v4, v140, v4
	v_add_f32_e32 v4, v142, v4
	v_add_f32_e32 v4, v138, v4
	s_waitcnt lgkmcnt(5)
	v_mfma_f32_32x32x16_f16 v[82:97], v[222:225], v[154:157], v[82:97]
	v_add_f32_e32 v4, v139, v4
	v_add_f32_e32 v4, v133, v4
	v_add_f32_e32 v4, v136, v4
	v_add_f32_e32 v4, v131, v4
	v_add_f32_e32 v4, v134, v4
	v_add_f32_e32 v4, v130, v4
	v_add_f32_e32 v4, v137, v4
	s_waitcnt lgkmcnt(3)
	v_mfma_f32_32x32x16_f16 v[98:113], v[230:233], v[158:161], v[98:113]
	v_add_f32_e32 v4, v132, v4
	v_add_f32_e32 v4, v135, v4
	v_add_f32_e32 v4, v2, v4
	v_add_f32_e32 v4, v16, v4
	v_add_f32_e32 v4, v17, v4
	v_add_f32_e32 v4, v114, v4
	v_add_f32_e32 v4, v115, v4
	s_waitcnt lgkmcnt(1)
	v_mfma_f32_32x32x16_f16 v[82:97], v[178:181], v[158:161], v[82:97]
	v_add_f32_e32 v4, v116, v4
	v_add_f32_e32 v4, v117, v4
	v_add_f32_e32 v4, v118, v4
	v_add_f32_e32 v4, v119, v4
	v_add_f32_e32 v4, v120, v4
	v_add_f32_e32 v4, v121, v4
	v_add_f32_e32 v4, v122, v4
	v_mfma_f32_32x32x16_f16 v[98:113], v[8:11], v[162:165], v[98:113]
	v_add_f32_e32 v4, v123, v4
	v_add_f32_e32 v4, v124, v4
	v_add_f32_e32 v4, v125, v4
	v_add_f32_e32 v222, v126, v4
	v_mov_b32_e32 v223, v222
	v_cvt_pk_f16_f32 v4, v143, v145
	v_cvt_pk_f16_f32 v5, v141, v144
	v_mfma_f32_32x32x16_f16 v[82:97], v[12:15], v[162:165], v[82:97]
	v_cvt_pk_f16_f32 v6, v140, v142
	v_cvt_pk_f16_f32 v7, v138, v139
	v_cvt_pk_f16_f32 v8, v133, v136
	v_cvt_pk_f16_f32 v9, v131, v134
	v_cvt_pk_f16_f32 v10, v130, v137
	v_cvt_pk_f16_f32 v11, v132, v135
	v_cvt_pk_f16_f32 v12, v2, v16
	v_mfma_f32_32x32x16_f16 v[98:113], v[182:185], v[166:169], v[98:113]
	v_cvt_pk_f16_f32 v13, v17, v114
	v_cvt_pk_f16_f32 v14, v115, v116
	v_cvt_pk_f16_f32 v15, v117, v118
	v_cvt_pk_f16_f32 v114, v119, v120
	v_cvt_pk_f16_f32 v115, v121, v122
	v_cvt_pk_f16_f32 v116, v123, v124
	v_cvt_pk_f16_f32 v117, v125, v126
	v_mfma_f32_32x32x16_f16 v[82:97], v[186:189], v[166:169], v[82:97]
	v_permlane32_swap_b32_e32 v222, v223
	v_permlane32_swap_b32_e32 v4, v6
	v_permlane32_swap_b32_e32 v5, v7
	v_permlane32_swap_b32_e32 v8, v10
	v_mfma_f32_32x32x16_f16 v[98:113], v[190:193], v[170:173], v[98:113]
	v_permlane32_swap_b32_e32 v9, v11
	v_permlane32_swap_b32_e32 v12, v14
	v_permlane32_swap_b32_e32 v13, v15
	v_permlane32_swap_b32_e32 v114, v116
	v_mfma_f32_32x32x16_f16 v[82:97], v[226:229], v[170:173], v[82:97]
	v_permlane32_swap_b32_e32 v115, v117
	v_mfma_f32_32x32x16_f16 v[98:113], v[234:237], v[174:177], v[98:113]
	s_waitcnt lgkmcnt(0)
	v_mfma_f32_32x32x16_f16 v[82:97], v[238:241], v[174:177], v[82:97]
	v_lshl_add_u64 v[204:205], s[30:31], 0, v[198:199]
	v_add_co_u32_e32 v16, vcc, s43, v204
	s_nop 1
	v_addc_co_u32_e32 v17, vcc, 0, v205, vcc
	v_add_co_u32_e32 v118, vcc, s44, v204
	s_nop 1
	v_addc_co_u32_e32 v119, vcc, 0, v205, vcc
	global_load_dwordx4 v[246:249], v[16:17], off
	global_load_dwordx4 v[250:253], v[118:119], off
	v_lshl_add_u64 v[16:17], s[28:29], 0, v[198:199]
	v_add_co_u32_e32 v118, vcc, s43, v16
	s_nop 1
	v_addc_co_u32_e32 v119, vcc, 0, v17, vcc
	v_add_co_u32_e32 v120, vcc, 0xa000, v16
	s_nop 1
	v_addc_co_u32_e32 v121, vcc, 0, v17, vcc
	global_load_dwordx4 v[186:189], v[118:119], off
	global_load_dwordx4 v[190:193], v[120:121], off
	s_add_i32 s34, s14, 0xffffff81
	s_sub_i32 s0, s14, 64
	s_cmp_le_i32 s0, s49
	s_cselect_b64 s[0:1], -1, 0
	s_cmp_gt_i32 s34, s50
	s_cselect_b64 s[34:35], -1, 0
	s_and_b64 s[0:1], s[34:35], s[0:1]
	s_and_b64 vcc, exec, s[0:1]
	s_cbranch_vccnz .LBB3_21
	v_add_u32_e32 v2, 0x87b, v221
	v_cmp_gt_u32_e32 vcc, s40, v2
	v_add_u32_e32 v2, 0x5b, v221
	s_nop 0
	v_cndmask_b32_e32 v98, v216, v98, vcc
	v_cmp_lt_u32_e32 vcc, s41, v2
	v_add_u32_e32 v2, 0x7a, v221
	s_nop 0
	v_cndmask_b32_e32 v82, v216, v82, vcc
	v_cmp_lt_u32_e32 vcc, s41, v2
	v_add_u32_e32 v2, 0x5a, v221
	s_nop 0
	v_cndmask_b32_e32 v99, v216, v99, vcc
	v_cmp_lt_u32_e32 vcc, s41, v2
	v_add_u32_e32 v2, 0x79, v221
	s_nop 0
	v_cndmask_b32_e32 v83, v216, v83, vcc
	v_cmp_lt_u32_e32 vcc, s41, v2
	v_add_u32_e32 v2, 0x59, v221
	s_nop 0
	v_cndmask_b32_e32 v100, v216, v100, vcc
	v_cmp_lt_u32_e32 vcc, s41, v2
	v_add_u32_e32 v2, 0x78, v221
	s_nop 0
	v_cndmask_b32_e32 v84, v216, v84, vcc
	v_cmp_lt_u32_e32 vcc, s41, v2
	v_add_u32_e32 v2, 0x58, v221
	s_nop 0
	v_cndmask_b32_e32 v101, v216, v101, vcc
	v_cmp_lt_u32_e32 vcc, s41, v2
	v_add_u32_e32 v2, 0x73, v221
	s_nop 0
	v_cndmask_b32_e32 v85, v216, v85, vcc
	v_cmp_lt_u32_e32 vcc, s41, v2
	v_add_u32_e32 v2, 0x53, v221
	s_nop 0
	v_cndmask_b32_e32 v102, v216, v102, vcc
	v_cmp_lt_u32_e32 vcc, s41, v2
	v_add_u32_e32 v2, 0x72, v221
	s_nop 0
	v_cndmask_b32_e32 v86, v216, v86, vcc
	v_cmp_lt_u32_e32 vcc, s41, v2
	v_add_u32_e32 v2, 0x52, v221
	s_nop 0
	v_cndmask_b32_e32 v103, v216, v103, vcc
	v_cmp_lt_u32_e32 vcc, s41, v2
	v_add_u32_e32 v2, 0x71, v221
	s_nop 0
	v_cndmask_b32_e32 v87, v216, v87, vcc
	v_cmp_lt_u32_e32 vcc, s41, v2
	v_add_u32_e32 v2, 0x51, v221
	s_nop 0
	v_cndmask_b32_e32 v104, v216, v104, vcc
	v_cmp_lt_u32_e32 vcc, s41, v2
	v_add_u32_e32 v2, 0x70, v221
	s_nop 0
	v_cndmask_b32_e32 v88, v216, v88, vcc
	v_cmp_lt_u32_e32 vcc, s41, v2
	v_add_u32_e32 v2, 0x50, v221
	s_nop 0
	v_cndmask_b32_e32 v105, v216, v105, vcc
	v_cmp_lt_u32_e32 vcc, s41, v2
	v_add_u32_e32 v2, 0x6b, v221
	s_nop 0
	v_cndmask_b32_e32 v89, v216, v89, vcc
	v_cmp_lt_u32_e32 vcc, s41, v2
	v_add_u32_e32 v2, 0x4b, v221
	s_nop 0
	v_cndmask_b32_e32 v106, v216, v106, vcc
	v_cmp_lt_u32_e32 vcc, s41, v2
	v_add_u32_e32 v2, 0x6a, v221
	s_nop 0
	v_cndmask_b32_e32 v90, v216, v90, vcc
	v_cmp_lt_u32_e32 vcc, s41, v2
	v_add_u32_e32 v2, 0x4a, v221
	s_nop 0
	v_cndmask_b32_e32 v107, v216, v107, vcc
	v_cmp_lt_u32_e32 vcc, s41, v2
	v_add_u32_e32 v2, 0x69, v221
	s_nop 0
	v_cndmask_b32_e32 v91, v216, v91, vcc
	v_cmp_lt_u32_e32 vcc, s41, v2
	v_add_u32_e32 v2, 0x49, v221
	s_nop 0
	v_cndmask_b32_e32 v108, v216, v108, vcc
	v_cmp_lt_u32_e32 vcc, s41, v2
	v_add_u32_e32 v2, 0x68, v221
	s_nop 0
	v_cndmask_b32_e32 v92, v216, v92, vcc
	v_cmp_lt_u32_e32 vcc, s41, v2
	v_add_u32_e32 v2, 0x48, v221
	s_nop 0
	v_cndmask_b32_e32 v109, v216, v109, vcc
	v_cmp_lt_u32_e32 vcc, s41, v2
	v_add_u32_e32 v2, 0x63, v221
	s_nop 0
	v_cndmask_b32_e32 v93, v216, v93, vcc
	v_cmp_lt_u32_e32 vcc, s41, v2
	v_add_u32_e32 v2, 0x43, v221
	s_nop 0
	v_cndmask_b32_e32 v110, v216, v110, vcc
	v_cmp_lt_u32_e32 vcc, s41, v2
	v_add_u32_e32 v2, 0x62, v221
	s_nop 0
	v_cndmask_b32_e32 v94, v216, v94, vcc
	v_cmp_lt_u32_e32 vcc, s41, v2
	v_add_u32_e32 v2, 0x42, v221
	s_nop 0
	v_cndmask_b32_e32 v111, v216, v111, vcc
	v_cmp_lt_u32_e32 vcc, s41, v2
	v_add_u32_e32 v2, 0x61, v221
	s_nop 0
	v_cndmask_b32_e32 v95, v216, v95, vcc
	v_cmp_lt_u32_e32 vcc, s41, v2
	v_add_u32_e32 v2, 0x41, v221
	s_nop 0
	v_cndmask_b32_e32 v112, v216, v112, vcc
	v_cmp_lt_u32_e32 vcc, s41, v2
	v_add_u32_e32 v2, 0x60, v221
	s_nop 0
	v_cndmask_b32_e32 v96, v216, v96, vcc
	v_cmp_lt_u32_e32 vcc, s41, v2
	v_add_u32_e32 v2, 64, v221
	s_nop 0
	v_cndmask_b32_e32 v113, v216, v113, vcc
	v_cmp_lt_u32_e32 vcc, s41, v2
	s_nop 1
	v_cndmask_b32_e32 v97, v216, v97, vcc
.LBB3_21:
	ds_read_b64_tr_b16 v[118:119], v207 offset:0
	ds_read_b64_tr_b16 v[120:121], v207 offset:0x800
	ds_read_b64_tr_b16 v[122:123], v207 offset:0x1000
	ds_read_b64_tr_b16 v[124:125], v207 offset:0x1800
	ds_read_b64_tr_b16 v[126:127], v207 offset:0x2000
	ds_read_b64_tr_b16 v[128:129], v207 offset:0x2800
	ds_read_b64_tr_b16 v[130:131], v207 offset:0x3000
	ds_read_b64_tr_b16 v[132:133], v207 offset:0x3800
	s_waitcnt lgkmcnt(0)
	s_nop 0
	v_mfma_f32_32x32x16_f16 v[66:81], v[118:121], v[4:7], v[66:81]
	v_max_f32_e32 v2, v99, v99
	v_max_f32_e32 v118, v98, v98
	v_max_f32_e32 v2, v118, v2
	v_max3_f32 v2, v2, v100, v101
	v_max3_f32 v2, v2, v102, v103
	v_max3_f32 v2, v2, v104, v105
	v_max3_f32 v2, v2, v106, v107
	v_mfma_f32_32x32x16_f16 v[66:81], v[122:125], v[8:11], v[66:81]
	v_max3_f32 v2, v2, v108, v109
	v_max3_f32 v2, v2, v110, v111
	v_max3_f32 v2, v2, v112, v113
	v_mfma_f32_32x32x16_f16 v[66:81], v[126:129], v[12:15], v[66:81]
	v_mfma_f32_32x32x16_f16 v[66:81], v[130:133], v[114:117], v[66:81]
	ds_read_b64_tr_b16 v[118:119], v207 offset:0x200
	ds_read_b64_tr_b16 v[120:121], v207 offset:0xa00
	ds_read_b64_tr_b16 v[122:123], v207 offset:0x1200
	ds_read_b64_tr_b16 v[124:125], v207 offset:0x1a00
	ds_read_b64_tr_b16 v[126:127], v207 offset:0x2200
	ds_read_b64_tr_b16 v[128:129], v207 offset:0x2a00
	ds_read_b64_tr_b16 v[130:131], v207 offset:0x3200
	ds_read_b64_tr_b16 v[132:133], v207 offset:0x3a00
	s_waitcnt lgkmcnt(0)
	s_nop 0
	v_mfma_f32_32x32x16_f16 v[50:65], v[118:121], v[4:7], v[50:65]
	v_max3_f32 v2, v2, v82, v83
	v_max3_f32 v2, v2, v84, v85
	v_max3_f32 v2, v2, v86, v87
	v_max3_f32 v2, v2, v88, v89
	v_max3_f32 v2, v2, v90, v91
	v_max3_f32 v2, v2, v92, v93
	v_max3_f32 v2, v2, v94, v95
	v_mfma_f32_32x32x16_f16 v[50:65], v[122:125], v[8:11], v[50:65]
	v_max3_f32 v2, v2, v96, v97
	v_mov_b32_e32 v118, v2
	s_nop 1
	v_permlane32_swap_b32_e32 v2, v118
	v_max_f32_e32 v118, v118, v118
	v_max_f32_e32 v2, v2, v2
	v_max_f32_e32 v2, v2, v118
	v_mfma_f32_32x32x16_f16 v[50:65], v[126:129], v[12:15], v[50:65]
	v_mfma_f32_32x32x16_f16 v[50:65], v[130:133], v[114:117], v[50:65]
	ds_read_b64_tr_b16 v[118:119], v207 offset:0x400
	ds_read_b64_tr_b16 v[120:121], v207 offset:0xc00
	ds_read_b64_tr_b16 v[122:123], v207 offset:0x1400
	ds_read_b64_tr_b16 v[124:125], v207 offset:0x1c00
	ds_read_b64_tr_b16 v[126:127], v207 offset:0x2400
	ds_read_b64_tr_b16 v[128:129], v207 offset:0x2c00
	ds_read_b64_tr_b16 v[130:131], v207 offset:0x3400
	ds_read_b64_tr_b16 v[132:133], v207 offset:0x3c00
	s_waitcnt lgkmcnt(0)
	s_nop 0
	v_mfma_f32_32x32x16_f16 v[34:49], v[118:121], v[4:7], v[34:49]
	v_sub_f32_e32 v118, v2, v194
	v_mul_f32_e32 v118, 0x3db504f3, v118
	v_cmp_ge_f32_e32 vcc, s42, v118
	s_cmp_eq_u64 vcc, exec
	v_max_f32_e32 v118, v194, v194
	v_max_f32_e32 v2, v118, v2
	s_cselect_b64 vcc, -1, 0
	v_mfma_f32_32x32x16_f16 v[34:49], v[122:125], v[8:11], v[34:49]
	v_cndmask_b32_e32 v226, v2, v194, vcc
	v_sub_f32_e32 v2, v194, v226
	v_mul_f32_e32 v2, 0x3e0293ee, v2
	v_exp_f32_e32 v2, v2
	s_nop 0
	v_cndmask_b32_e64 v2, v2, 1.0, vcc
	v_mfma_f32_32x32x16_f16 v[34:49], v[126:129], v[12:15], v[34:49]
	v_mfma_f32_32x32x16_f16 v[34:49], v[130:133], v[114:117], v[34:49]
	ds_read_b64_tr_b16 v[118:119], v207 offset:0x600
	ds_read_b64_tr_b16 v[120:121], v207 offset:0xe00
	ds_read_b64_tr_b16 v[122:123], v207 offset:0x1600
	ds_read_b64_tr_b16 v[124:125], v207 offset:0x1e00
	ds_read_b64_tr_b16 v[126:127], v207 offset:0x2600
	ds_read_b64_tr_b16 v[128:129], v207 offset:0x2e00
	ds_read_b64_tr_b16 v[130:131], v207 offset:0x3600
	ds_read_b64_tr_b16 v[132:133], v207 offset:0x3e00
	s_waitcnt lgkmcnt(0)
	s_nop 0
	v_mfma_f32_32x32x16_f16 v[18:33], v[118:121], v[4:7], v[18:33]
	v_mfma_f32_32x32x16_f16 v[18:33], v[122:125], v[8:11], v[18:33]
	v_mfma_f32_32x32x16_f16 v[18:33], v[126:129], v[12:15], v[18:33]
	v_mfma_f32_32x32x16_f16 v[18:33], v[130:133], v[114:117], v[18:33]
	s_waitcnt vmcnt(0)
	v_cmp_gt_f32_e32 vcc, 1.0, v2
	s_waitcnt vmcnt(1)
	ds_write_b128 v214, v[186:189] offset:32768
	s_waitcnt vmcnt(0)
	ds_write_b128 v214, v[190:193] offset:40960
	s_cbranch_vccz .LBB3_23
	v_pk_mul_f32 v[80:81], v[80:81], v[2:3] op_sel_hi:[1,0]
	v_pk_mul_f32 v[78:79], v[78:79], v[2:3] op_sel_hi:[1,0]
	v_pk_mul_f32 v[76:77], v[76:77], v[2:3] op_sel_hi:[1,0]
	v_pk_mul_f32 v[74:75], v[74:75], v[2:3] op_sel_hi:[1,0]
	v_pk_mul_f32 v[72:73], v[72:73], v[2:3] op_sel_hi:[1,0]
	v_pk_mul_f32 v[70:71], v[70:71], v[2:3] op_sel_hi:[1,0]
	v_pk_mul_f32 v[68:69], v[68:69], v[2:3] op_sel_hi:[1,0]
	v_pk_mul_f32 v[66:67], v[66:67], v[2:3] op_sel_hi:[1,0]
	v_pk_mul_f32 v[64:65], v[64:65], v[2:3] op_sel_hi:[1,0]
	v_pk_mul_f32 v[62:63], v[62:63], v[2:3] op_sel_hi:[1,0]
	v_pk_mul_f32 v[60:61], v[60:61], v[2:3] op_sel_hi:[1,0]
	v_pk_mul_f32 v[58:59], v[58:59], v[2:3] op_sel_hi:[1,0]
	v_pk_mul_f32 v[56:57], v[56:57], v[2:3] op_sel_hi:[1,0]
	v_pk_mul_f32 v[54:55], v[54:55], v[2:3] op_sel_hi:[1,0]
	v_pk_mul_f32 v[52:53], v[52:53], v[2:3] op_sel_hi:[1,0]
	v_pk_mul_f32 v[50:51], v[50:51], v[2:3] op_sel_hi:[1,0]
	v_pk_mul_f32 v[48:49], v[48:49], v[2:3] op_sel_hi:[1,0]
	v_pk_mul_f32 v[46:47], v[46:47], v[2:3] op_sel_hi:[1,0]
	v_pk_mul_f32 v[44:45], v[44:45], v[2:3] op_sel_hi:[1,0]
	v_pk_mul_f32 v[42:43], v[42:43], v[2:3] op_sel_hi:[1,0]
	v_pk_mul_f32 v[40:41], v[40:41], v[2:3] op_sel_hi:[1,0]
	v_pk_mul_f32 v[38:39], v[38:39], v[2:3] op_sel_hi:[1,0]
	v_pk_mul_f32 v[36:37], v[36:37], v[2:3] op_sel_hi:[1,0]
	v_pk_mul_f32 v[34:35], v[34:35], v[2:3] op_sel_hi:[1,0]
	v_pk_mul_f32 v[32:33], v[2:3], v[32:33] op_sel_hi:[0,1]
	v_pk_mul_f32 v[30:31], v[2:3], v[30:31] op_sel_hi:[0,1]
	v_pk_mul_f32 v[28:29], v[2:3], v[28:29] op_sel_hi:[0,1]
	v_pk_mul_f32 v[26:27], v[2:3], v[26:27] op_sel_hi:[0,1]
	v_pk_mul_f32 v[24:25], v[2:3], v[24:25] op_sel_hi:[0,1]
	v_pk_mul_f32 v[22:23], v[2:3], v[22:23] op_sel_hi:[0,1]
	v_pk_mul_f32 v[20:21], v[2:3], v[20:21] op_sel_hi:[0,1]
	v_pk_mul_f32 v[18:19], v[2:3], v[18:19] op_sel_hi:[0,1]
.LBB3_23:
	v_mul_f32_e32 v12, 0xbe0293ee, v226
	v_fmamk_f32 v4, v98, 0x3e0293ee, v12
	v_fmamk_f32 v5, v99, 0x3e0293ee, v12
	v_fmamk_f32 v6, v100, 0x3e0293ee, v12
	v_fmamk_f32 v7, v101, 0x3e0293ee, v12
	v_fmamk_f32 v8, v102, 0x3e0293ee, v12
	v_fmamk_f32 v9, v103, 0x3e0293ee, v12
	v_fmamk_f32 v10, v104, 0x3e0293ee, v12
	v_fmamk_f32 v11, v105, 0x3e0293ee, v12
	v_fmamk_f32 v13, v106, 0x3e0293ee, v12
	v_fmamk_f32 v14, v107, 0x3e0293ee, v12
	v_fmamk_f32 v15, v108, 0x3e0293ee, v12
	v_fmamk_f32 v98, v109, 0x3e0293ee, v12
	v_fmamk_f32 v99, v110, 0x3e0293ee, v12
	v_fmamk_f32 v100, v111, 0x3e0293ee, v12
	v_fmamk_f32 v101, v112, 0x3e0293ee, v12
	v_fmamk_f32 v102, v113, 0x3e0293ee, v12
	v_fmamk_f32 v103, v82, 0x3e0293ee, v12
	v_fmamk_f32 v104, v83, 0x3e0293ee, v12
	v_fmamk_f32 v105, v84, 0x3e0293ee, v12
	v_fmamk_f32 v106, v85, 0x3e0293ee, v12
	v_fmamk_f32 v107, v86, 0x3e0293ee, v12
	v_fmamk_f32 v108, v87, 0x3e0293ee, v12
	v_fmamk_f32 v109, v88, 0x3e0293ee, v12
	v_fmamk_f32 v110, v89, 0x3e0293ee, v12
	v_fmamk_f32 v111, v90, 0x3e0293ee, v12
	v_fmamk_f32 v112, v91, 0x3e0293ee, v12
	v_fmamk_f32 v113, v92, 0x3e0293ee, v12
	v_fmamk_f32 v194, v93, 0x3e0293ee, v12
	v_fmamk_f32 v195, v94, 0x3e0293ee, v12
	v_fmamk_f32 v196, v95, 0x3e0293ee, v12
	v_fmamk_f32 v197, v96, 0x3e0293ee, v12
	v_fmac_f32_e32 v12, 0x3e0293ee, v97
	v_exp_f32_e32 v82, v4
	v_exp_f32_e32 v83, v5
	v_exp_f32_e32 v84, v6
	v_exp_f32_e32 v85, v7
	v_exp_f32_e32 v86, v8
	v_exp_f32_e32 v87, v9
	v_exp_f32_e32 v88, v10
	v_exp_f32_e32 v89, v11
	v_exp_f32_e32 v90, v13
	v_exp_f32_e32 v91, v14
	v_exp_f32_e32 v92, v15
	v_exp_f32_e32 v93, v98
	v_exp_f32_e32 v94, v99
	v_exp_f32_e32 v95, v100
	v_exp_f32_e32 v96, v101
	v_exp_f32_e32 v97, v102
	s_waitcnt lgkmcnt(0)
	s_barrier
	ds_write_b128 v212, v[246:249]
	ds_write_b128 v213, v[250:253]
	ds_read_b128 v[4:7], v208 offset:32768
	ds_read_b128 v[8:11], v208 offset:40960
	v_exp_f32_e32 v98, v103
	v_exp_f32_e32 v99, v104
	v_exp_f32_e32 v100, v105
	s_waitcnt lgkmcnt(1)
	v_mfma_f32_32x32x16_f16 v[130:145], v[4:7], v[146:149], 0
	v_exp_f32_e32 v101, v106
	v_exp_f32_e32 v102, v107
	v_exp_f32_e32 v103, v108
	v_exp_f32_e32 v104, v109
	v_exp_f32_e32 v105, v110
	v_exp_f32_e32 v106, v111
	v_exp_f32_e32 v107, v112
	s_waitcnt lgkmcnt(0)
	v_mfma_f32_32x32x16_f16 v[114:129], v[8:11], v[146:149], 0
	ds_read_b128 v[4:7], v209 offset:32768
	ds_read_b128 v[8:11], v209 offset:40960
	v_exp_f32_e32 v108, v113
	v_exp_f32_e32 v109, v194
	v_exp_f32_e32 v110, v195
	v_exp_f32_e32 v111, v196
	v_exp_f32_e32 v112, v197
	v_exp_f32_e32 v113, v12
	s_waitcnt lgkmcnt(1)
	v_mfma_f32_32x32x16_f16 v[130:145], v[4:7], v[150:153], v[130:145]
	s_waitcnt lgkmcnt(0)
	v_mfma_f32_32x32x16_f16 v[114:129], v[8:11], v[150:153], v[114:129]
	ds_read_b128 v[4:7], v210 offset:32768
	ds_read_b128 v[8:11], v210 offset:40960
	s_waitcnt lgkmcnt(1)
	v_mfma_f32_32x32x16_f16 v[130:145], v[4:7], v[154:157], v[130:145]
	s_waitcnt lgkmcnt(0)
	v_mfma_f32_32x32x16_f16 v[114:129], v[8:11], v[154:157], v[114:129]
	ds_read_b128 v[4:7], v211 offset:32768
	ds_read_b128 v[8:11], v211 offset:40960
	s_waitcnt lgkmcnt(1)
	v_mfma_f32_32x32x16_f16 v[130:145], v[4:7], v[158:161], v[130:145]
	s_waitcnt lgkmcnt(0)
	v_mfma_f32_32x32x16_f16 v[114:129], v[8:11], v[158:161], v[114:129]
	ds_read_b128 v[4:7], v208 offset:32896
	ds_read_b128 v[8:11], v208 offset:41088
	s_waitcnt lgkmcnt(1)
	v_mfma_f32_32x32x16_f16 v[130:145], v[4:7], v[162:165], v[130:145]
	s_waitcnt lgkmcnt(0)
	v_mfma_f32_32x32x16_f16 v[114:129], v[8:11], v[162:165], v[114:129]
	ds_read_b128 v[4:7], v209 offset:32896
	ds_read_b128 v[8:11], v209 offset:41088
	s_waitcnt lgkmcnt(1)
	v_mfma_f32_32x32x16_f16 v[130:145], v[4:7], v[166:169], v[130:145]
	s_waitcnt lgkmcnt(0)
	v_mfma_f32_32x32x16_f16 v[114:129], v[8:11], v[166:169], v[114:129]
	ds_read_b128 v[4:7], v210 offset:32896
	ds_read_b128 v[8:11], v210 offset:41088
	s_waitcnt lgkmcnt(1)
	v_mfma_f32_32x32x16_f16 v[130:145], v[4:7], v[170:173], v[130:145]
	s_waitcnt lgkmcnt(0)
	v_mfma_f32_32x32x16_f16 v[114:129], v[8:11], v[170:173], v[114:129]
	ds_read_b128 v[4:7], v211 offset:32896
	ds_read_b128 v[8:11], v211 offset:41088
	s_waitcnt lgkmcnt(1)
	v_mfma_f32_32x32x16_f16 v[130:145], v[4:7], v[174:177], v[130:145]
	v_add_f32_e32 v4, 0, v82
	v_add_f32_e32 v4, v83, v4
	v_add_f32_e32 v4, v84, v4
	v_add_f32_e32 v4, v85, v4
	v_add_f32_e32 v4, v86, v4
	v_add_f32_e32 v4, v87, v4
	v_add_f32_e32 v4, v88, v4
	v_add_f32_e32 v4, v89, v4
	v_add_f32_e32 v4, v90, v4
	v_add_f32_e32 v4, v91, v4
	v_add_f32_e32 v4, v92, v4
	v_add_f32_e32 v4, v93, v4
	v_add_f32_e32 v4, v94, v4
	v_add_f32_e32 v4, v95, v4
	v_add_f32_e32 v4, v96, v4
	v_add_f32_e32 v4, v97, v4
	v_add_f32_e32 v4, v98, v4
	v_add_f32_e32 v4, v99, v4
	v_add_f32_e32 v4, v100, v4
	v_add_f32_e32 v4, v101, v4
	v_add_f32_e32 v4, v102, v4
	v_add_f32_e32 v4, v103, v4
	v_add_f32_e32 v4, v104, v4
	v_add_f32_e32 v4, v105, v4
	v_add_f32_e32 v4, v106, v4
	v_add_f32_e32 v4, v107, v4
	s_waitcnt lgkmcnt(0)
	v_mfma_f32_32x32x16_f16 v[114:129], v[8:11], v[174:177], v[114:129]
	v_add_f32_e32 v4, v108, v4
	v_add_f32_e32 v4, v109, v4
	v_add_f32_e32 v4, v110, v4
	v_add_f32_e32 v4, v111, v4
	v_add_f32_e32 v4, v112, v4
	v_add_f32_e32 v224, v113, v4
	v_mov_b32_e32 v225, v224
	v_cvt_pk_f16_f32 v4, v82, v83
	v_cvt_pk_f16_f32 v5, v84, v85
	v_cvt_pk_f16_f32 v6, v86, v87
	v_cvt_pk_f16_f32 v7, v88, v89
	v_cvt_pk_f16_f32 v8, v90, v91
	v_cvt_pk_f16_f32 v9, v92, v93
	v_cvt_pk_f16_f32 v10, v94, v95
	v_cvt_pk_f16_f32 v11, v96, v97
	v_cvt_pk_f16_f32 v12, v98, v99
	v_cvt_pk_f16_f32 v13, v100, v101
	v_cvt_pk_f16_f32 v14, v102, v103
	v_cvt_pk_f16_f32 v15, v104, v105
	v_cvt_pk_f16_f32 v194, v106, v107
	v_cvt_pk_f16_f32 v195, v108, v109
	v_cvt_pk_f16_f32 v196, v110, v111
	v_cvt_pk_f16_f32 v197, v112, v113
	s_nop 1
	v_permlane32_swap_b32_e32 v224, v225
	v_permlane32_swap_b32_e32 v4, v6
	v_permlane32_swap_b32_e32 v5, v7
	v_permlane32_swap_b32_e32 v8, v10
	v_permlane32_swap_b32_e32 v9, v11
	v_permlane32_swap_b32_e32 v12, v14
	v_permlane32_swap_b32_e32 v13, v15
	v_permlane32_swap_b32_e32 v194, v196
	v_permlane32_swap_b32_e32 v195, v197
	s_add_i32 s0, s51, 1
	s_cmp_lt_i32 s0, s48
	s_cselect_b64 s[34:35], -1, 0
	s_cmp_ge_i32 s0, s48
	s_cbranch_scc1 .LBB3_25
	v_add_co_u32_e32 v178, vcc, 0xc000, v204
	s_nop 1
	v_addc_co_u32_e32 v179, vcc, 0, v205, vcc
	v_add_co_u32_e32 v180, vcc, 0xe000, v204
	s_nop 1
	v_addc_co_u32_e32 v181, vcc, 0, v205, vcc
	v_add_co_u32_e32 v186, vcc, 0xc000, v16
	global_load_dwordx4 v[246:249], v[178:179], off
	s_nop 0
	global_load_dwordx4 v[250:253], v[180:181], off
	v_addc_co_u32_e32 v187, vcc, 0, v17, vcc
	v_add_co_u32_e32 v16, vcc, 0xe000, v16
	s_nop 1
	v_addc_co_u32_e32 v17, vcc, 0, v17, vcc
	global_load_dwordx4 v[186:189], v[186:187], off
	s_nop 0
	global_load_dwordx4 v[190:193], v[16:17], off

.LBB3_27:
	ds_read_b64_tr_b16 v[228:229], v207 offset:0x4000
	ds_read_b64_tr_b16 v[230:231], v207 offset:0x4800
	ds_read_b64_tr_b16 v[232:233], v207 offset:0x5000
	ds_read_b64_tr_b16 v[234:235], v207 offset:0x5800
	ds_read_b64_tr_b16 v[236:237], v207 offset:0x6000
	ds_read_b64_tr_b16 v[238:239], v207 offset:0x6800
	ds_read_b64_tr_b16 v[240:241], v207 offset:0x7000
	ds_read_b64_tr_b16 v[242:243], v207 offset:0x7800
	s_waitcnt lgkmcnt(0)
	s_nop 0
	v_mfma_f32_32x32x16_f16 v[66:81], v[228:231], v[4:7], v[66:81]
	v_max_f32_e32 v16, v131, v131
	v_max_f32_e32 v17, v130, v130
	v_max_f32_e32 v16, v17, v16
	v_max3_f32 v16, v16, v132, v133
	v_max3_f32 v16, v16, v134, v135
	v_max3_f32 v16, v16, v136, v137
	v_max3_f32 v16, v16, v138, v139
	v_mfma_f32_32x32x16_f16 v[66:81], v[232:235], v[8:11], v[66:81]
	v_max3_f32 v16, v16, v140, v141
	v_max3_f32 v16, v16, v142, v143
	v_max3_f32 v16, v16, v144, v145
	v_mfma_f32_32x32x16_f16 v[66:81], v[236:239], v[12:15], v[66:81]
	v_mfma_f32_32x32x16_f16 v[66:81], v[240:243], v[194:197], v[66:81]
	ds_read_b64_tr_b16 v[228:229], v207 offset:0x4200
	ds_read_b64_tr_b16 v[230:231], v207 offset:0x4a00
	ds_read_b64_tr_b16 v[232:233], v207 offset:0x5200
	ds_read_b64_tr_b16 v[234:235], v207 offset:0x5a00
	ds_read_b64_tr_b16 v[236:237], v207 offset:0x6200
	ds_read_b64_tr_b16 v[238:239], v207 offset:0x6a00
	ds_read_b64_tr_b16 v[240:241], v207 offset:0x7200
	ds_read_b64_tr_b16 v[242:243], v207 offset:0x7a00
	s_waitcnt lgkmcnt(0)
	s_nop 0
	v_mfma_f32_32x32x16_f16 v[50:65], v[228:231], v[4:7], v[50:65]
	v_max3_f32 v16, v16, v114, v115
	v_max3_f32 v16, v16, v116, v117
	v_max3_f32 v16, v16, v118, v119
	v_max3_f32 v16, v16, v120, v121
	v_max3_f32 v16, v16, v122, v123
	v_max3_f32 v16, v16, v124, v125
	v_max3_f32 v16, v16, v126, v127
	v_mfma_f32_32x32x16_f16 v[50:65], v[232:235], v[8:11], v[50:65]
	v_max3_f32 v16, v16, v128, v129
	v_mov_b32_e32 v17, v16
	s_nop 1
	v_permlane32_swap_b32_e32 v16, v17
	v_max_f32_e32 v17, v17, v17
	v_max_f32_e32 v16, v16, v16
	v_max_f32_e32 v16, v16, v17
	v_mfma_f32_32x32x16_f16 v[50:65], v[236:239], v[12:15], v[50:65]
	v_mfma_f32_32x32x16_f16 v[50:65], v[240:243], v[194:197], v[50:65]
	ds_read_b64_tr_b16 v[228:229], v207 offset:0x4400
	ds_read_b64_tr_b16 v[230:231], v207 offset:0x4c00
	ds_read_b64_tr_b16 v[232:233], v207 offset:0x5400
	ds_read_b64_tr_b16 v[234:235], v207 offset:0x5c00
	ds_read_b64_tr_b16 v[236:237], v207 offset:0x6400
	ds_read_b64_tr_b16 v[238:239], v207 offset:0x6c00
	ds_read_b64_tr_b16 v[240:241], v207 offset:0x7400
	ds_read_b64_tr_b16 v[242:243], v207 offset:0x7c00
	s_waitcnt lgkmcnt(0)
	s_nop 0
	v_mfma_f32_32x32x16_f16 v[34:49], v[228:231], v[4:7], v[34:49]
	v_sub_f32_e32 v17, v16, v226
	v_mul_f32_e32 v17, 0x3db504f3, v17
	v_cmp_ge_f32_e32 vcc, s42, v17
	s_cmp_eq_u64 vcc, exec
	s_cselect_b64 s[0:1], -1, 0
	v_mfma_f32_32x32x16_f16 v[34:49], v[232:235], v[8:11], v[34:49]
	v_mfma_f32_32x32x16_f16 v[34:49], v[236:239], v[12:15], v[34:49]
	v_mfma_f32_32x32x16_f16 v[34:49], v[240:243], v[194:197], v[34:49]
	ds_read_b64_tr_b16 v[228:229], v207 offset:0x4600
	ds_read_b64_tr_b16 v[230:231], v207 offset:0x4e00
	ds_read_b64_tr_b16 v[232:233], v207 offset:0x5600
	ds_read_b64_tr_b16 v[234:235], v207 offset:0x5e00
	ds_read_b64_tr_b16 v[236:237], v207 offset:0x6600
	ds_read_b64_tr_b16 v[238:239], v207 offset:0x6e00
	ds_read_b64_tr_b16 v[240:241], v207 offset:0x7600
	ds_read_b64_tr_b16 v[242:243], v207 offset:0x7e00
	s_waitcnt lgkmcnt(0)
	s_nop 0
	v_mfma_f32_32x32x16_f16 v[18:33], v[228:231], v[4:7], v[18:33]
	v_mfma_f32_32x32x16_f16 v[18:33], v[232:235], v[8:11], v[18:33]
	v_mfma_f32_32x32x16_f16 v[18:33], v[236:239], v[12:15], v[18:33]
	v_mfma_f32_32x32x16_f16 v[18:33], v[240:243], v[194:197], v[18:33]
	s_andn2_b64 vcc, exec, s[34:35]
	s_cbranch_vccnz .LBB3_29
	s_waitcnt vmcnt(0)
	s_waitcnt vmcnt(1)
	ds_write_b128 v214, v[186:189] offset:49152
	s_waitcnt vmcnt(0)
	ds_write_b128 v214, v[190:193] offset:57344

.Lattn_flush:
	s_andn2_b64 vcc, exec, s[34:35]
	s_cbranch_vccnz .LBB3_32
	ds_write_b128 v212, v[246:249] offset:16384
	ds_write_b128 v213, v[250:253] offset:16384
	s_waitcnt lgkmcnt(0)
	s_barrier
	s_branch .LBB3_32

	.amdhsa_kernel _Z11attn_kernelPKDF16_PDF16_
		.amdhsa_group_segment_fixed_size 0
		.amdhsa_private_segment_fixed_size 0
		.amdhsa_kernarg_size 272
		.amdhsa_user_sgpr_count 2
		.amdhsa_user_sgpr_dispatch_ptr 0
		.amdhsa_user_sgpr_queue_ptr 0
		.amdhsa_user_sgpr_kernarg_segment_ptr 1
		.amdhsa_user_sgpr_dispatch_id 0
		.amdhsa_user_sgpr_kernarg_preload_length 0
		.amdhsa_user_sgpr_kernarg_preload_offset 0
		.amdhsa_user_sgpr_private_segment_size 0
		.amdhsa_uses_dynamic_stack 0
		.amdhsa_enable_private_segment 0
		.amdhsa_system_sgpr_workgroup_id_x 1
		.amdhsa_system_sgpr_workgroup_id_y 0
		.amdhsa_system_sgpr_workgroup_id_z 0
		.amdhsa_system_sgpr_workgroup_info 0
		.amdhsa_system_vgpr_workitem_id 0
		.amdhsa_next_free_vgpr 256
		.amdhsa_next_free_sgpr 54
		.amdhsa_accum_offset 256
		.amdhsa_reserve_vcc 1
		.amdhsa_float_round_mode_32 0
		.amdhsa_float_round_mode_16_64 0
		.amdhsa_float_denorm_mode_32 3
		.amdhsa_float_denorm_mode_16_64 3
		.amdhsa_dx10_clamp 1
		.amdhsa_ieee_mode 1
		.amdhsa_fp16_overflow 0
		.amdhsa_tg_split 0
		.amdhsa_exception_fp_ieee_invalid_op 0
		.amdhsa_exception_fp_denorm_src 0
		.amdhsa_exception_fp_ieee_div_zero 0
		.amdhsa_exception_fp_ieee_overflow 0
		.amdhsa_exception_fp_ieee_underflow 0
		.amdhsa_exception_fp_ieee_inexact 0
		.amdhsa_exception_int_div_zero 0
	.end_amdhsa_kernel

amdhsa.kernels:
  - .agpr_count:     0
    .args:
      - .actual_access:  read_only
        .address_space:  global
        .offset:         0
        .size:           8
        .value_kind:     global_buffer
      - .actual_access:  read_only
        .address_space:  global
        .offset:         8
        .size:           8
        .value_kind:     global_buffer
      - .actual_access:  read_only
        .address_space:  global
        .offset:         16
        .size:           8
        .value_kind:     global_buffer
      - .actual_access:  read_only
        .address_space:  global
        .offset:         24
        .size:           8
        .value_kind:     global_buffer
      - .actual_access:  read_only
        .address_space:  global
        .offset:         32
        .size:           8
        .value_kind:     global_buffer
      - .address_space:  global
        .offset:         40
        .size:           8
        .value_kind:     global_buffer
      - .address_space:  global
        .offset:         48
        .size:           8
        .value_kind:     global_buffer
      - .address_space:  global
        .offset:         56
        .size:           8
        .value_kind:     global_buffer
      - .actual_access:  write_only
        .address_space:  global
        .offset:         64
        .size:           8
        .value_kind:     global_buffer
    .group_segment_fixed_size: 0
    .kernarg_segment_align: 8
    .kernarg_segment_size: 72
    .language:       OpenCL C
    .language_version:
      - 2
      - 0
    .max_flat_workgroup_size: 256
    .name:           _Z10cvt_kernelPKfS0_S0_S0_S0_PDF16_S1_S1_P15HIP_vector_typeIfLj2EE
    .private_segment_fixed_size: 0
    .sgpr_count:     30
    .sgpr_spill_count: 0
    .symbol:         _Z10cvt_kernelPKfS0_S0_S0_S0_PDF16_S1_S1_P15HIP_vector_typeIfLj2EE.kd
    .uniform_work_group_size: 1
    .uses_dynamic_stack: false
    .vgpr_count:     21
    .vgpr_spill_count: 0
    .wavefront_size: 64
  - .agpr_count:     0
    .args:
      - .address_space:  global
        .offset:         0
        .size:           8
        .value_kind:     global_buffer
      - .address_space:  global
        .offset:         8
        .size:           8
        .value_kind:     global_buffer
      - .address_space:  global
        .offset:         16
        .size:           8
        .value_kind:     global_buffer
      - .offset:         24
        .size:           4
        .value_kind:     by_value
      - .offset:         28
        .size:           4
        .value_kind:     by_value
      - .offset:         32
        .size:           4
        .value_kind:     by_value
    .group_segment_fixed_size: 0
    .kernarg_segment_align: 8
    .kernarg_segment_size: 36
    .language:       OpenCL C
    .language_version:
      - 2
      - 0
    .max_flat_workgroup_size: 512
    .name:           _Z15gemm_out_kernelPKDF16_S0_Pfiii
    .private_segment_fixed_size: 0
    .sgpr_count:     42
    .sgpr_spill_count: 0
    .symbol:         _Z15gemm_out_kernelPKDF16_S0_Pfiii.kd
    .uniform_work_group_size: 1
    .uses_dynamic_stack: false
    .vgpr_count:     247
    .vgpr_spill_count: 0
    .wavefront_size: 64
  - .agpr_count:     0
    .args:
      - .address_space:  global
        .offset:         0
        .size:           8
        .value_kind:     global_buffer
      - .address_space:  global
        .offset:         8
        .size:           8
        .value_kind:     global_buffer
      - .address_space:  global
        .offset:         16
        .size:           8
        .value_kind:     global_buffer
      - .actual_access:  read_only
        .address_space:  global
        .offset:         24
        .size:           8
        .value_kind:     global_buffer
      - .actual_access:  read_only
        .address_space:  global
        .offset:         32
        .size:           8
        .value_kind:     global_buffer
      - .actual_access:  read_only
        .address_space:  global
        .offset:         40
        .size:           8
        .value_kind:     global_buffer
    .group_segment_fixed_size: 0
    .kernarg_segment_align: 8
    .kernarg_segment_size: 48
    .language:       OpenCL C
    .language_version:
      - 2
      - 0
    .max_flat_workgroup_size: 512
    .name:           _Z15gemm_qkv_kernelPKDF16_S0_PDF16_PKfS3_PK15HIP_vector_typeIfLj2EE
    .private_segment_fixed_size: 0
    .sgpr_count:     49
    .sgpr_spill_count: 0
    .symbol:         _Z15gemm_qkv_kernelPKDF16_S0_PDF16_PKfS3_PK15HIP_vector_typeIfLj2EE.kd
    .uniform_work_group_size: 1
    .uses_dynamic_stack: false
    .vgpr_count:     226
    .vgpr_spill_count: 0
    .wavefront_size: 64
  - .agpr_count:     0
    .args:
      - .actual_access:  read_only
        .address_space:  global
        .offset:         0
        .size:           8
        .value_kind:     global_buffer
      - .actual_access:  write_only
        .address_space:  global
        .offset:         8
        .size:           8
        .value_kind:     global_buffer
      - .offset:         16
        .size:           4
        .value_kind:     hidden_block_count_x
      - .offset:         20
        .size:           4
        .value_kind:     hidden_block_count_y
      - .offset:         24
        .size:           4
        .value_kind:     hidden_block_count_z
      - .offset:         28
        .size:           2
        .value_kind:     hidden_group_size_x
      - .offset:         30
        .size:           2
        .value_kind:     hidden_group_size_y
      - .offset:         32
        .size:           2
        .value_kind:     hidden_group_size_z
      - .offset:         34
        .size:           2
        .value_kind:     hidden_remainder_x
      - .offset:         36
        .size:           2
        .value_kind:     hidden_remainder_y
      - .offset:         38
        .size:           2
        .value_kind:     hidden_remainder_z
      - .offset:         56
        .size:           8
        .value_kind:     hidden_global_offset_x
      - .offset:         64
        .size:           8
        .value_kind:     hidden_global_offset_y
      - .offset:         72
        .size:           8
        .value_kind:     hidden_global_offset_z
      - .offset:         80
        .size:           2
        .value_kind:     hidden_grid_dims
      - .offset:         136
        .size:           4
        .value_kind:     hidden_dynamic_lds_size
    .group_segment_fixed_size: 0
    .kernarg_segment_align: 8
    .kernarg_segment_size: 272
    .language:       OpenCL C
    .language_version:
      - 2
      - 0
    .max_flat_workgroup_size: 512
    .name:           _Z11attn_kernelPKDF16_PDF16_
    .private_segment_fixed_size: 0
    .sgpr_count:     60
    .sgpr_spill_count: 0
    .symbol:         _Z11attn_kernelPKDF16_PDF16_.kd
    .uniform_work_group_size: 1
    .uses_dynamic_stack: false
    .vgpr_count:     256
    .vgpr_spill_count: 0
    .wavefront_size: 64
